# v29
# speedup vs baseline: 1.0076x; 1.0076x over previous
_Z7k_layerILb1EEvPKvPKhPKfPKiS7_PKDF16_S5_PvPhPf:
	s_load_dwordx8 s[8:15], s[0:1], 0x0
	s_load_dwordx4 s[4:7], s[0:1], 0x20
	s_load_dwordx2 s[16:17], s[0:1], 0x30
	v_and_b32_e32 v68, 63, v0
	v_lshrrev_b32_e32 v72, 6, v0
	v_bfe_u32 v1, v0, 4, 2
	v_and_b32_e32 v73, 15, v0
	s_setprio 3
	s_mul_i32 s18, s2, 60
	v_and_b32_e32 v75, 31, v0
	v_mad_u32_u24 v78, v72, 15, s18
	v_min_u32_e32 v2, 15, v75
	v_add_u32_e32 v2, v78, v2
	v_min_i32_e32 v2, 0x186a0, v2
	v_ashrrev_i32_e32 v3, 31, v2
	s_waitcnt lgkmcnt(0)
	v_lshl_add_u64 v[2:3], v[2:3], 2, s[14:15]
	global_load_dword v22, v[2:3], off
	v_lshl_or_b32 v74, v72, 5, v75
	v_lshlrev_b32_e32 v2, 2, v74
	global_load_dword v67, v2, s[16:17]
	v_and_b32_e32 v2, 0xc0, v0
	v_mov_b32_e32 v9, 0
	v_lshlrev_b32_e32 v8, 4, v2
	v_lshl_add_u64 v[10:11], s[6:7], 0, v[8:9]
	v_mul_u32_u24_e32 v77, 15, v72
	s_mov_b32 s16, 0x186a0
	s_mov_b32 s17, 0
	s_mov_b64 s[2:3], -1
	v_mbcnt_lo_u32_b32 v23, -1, 0
	v_add_u32_e32 v76, v1, v77
	v_lshlrev_b32_e32 v8, 4, v68
	v_lshlrev_b32_e32 v66, 3, v73
	v_lshlrev_b32_e32 v6, 5, v73
	s_waitcnt vmcnt(1)
	v_readlane_b32 s6, v22, 0
	v_readlane_b32 s7, v22, 16
	s_sub_i32 s19, s7, s6
	s_cmpk_lt_i32 s19, 0x181
	s_cbranch_scc1 .LBB2_12
	v_mbcnt_hi_u32_b32 v2, -1, v23
	v_and_b32_e32 v24, 64, v2
	v_mov_b32_e32 v7, v9
	v_or_b32_e32 v25, 1, v24
	v_lshl_add_u64 v[12:13], s[8:9], 0, v[6:7]
	s_mov_b32 s7, 0x64646464
	v_mov_b32_e32 v7, 0x4010400
	v_mov_b32_e32 v26, 0x4030402
	s_branch .LBB2_4

_Z7k_layerILb0EEvPKvPKhPKfPKiS7_PKDF16_S5_PvPhPf:
	s_load_dwordx8 s[8:15], s[0:1], 0x0
	s_load_dwordx4 s[4:7], s[0:1], 0x20
	s_load_dwordx2 s[18:19], s[0:1], 0x30
	v_and_b32_e32 v66, 63, v0
	v_lshrrev_b32_e32 v18, 6, v0
	v_bfe_u32 v73, v0, 4, 2
	v_and_b32_e32 v71, 15, v0
	s_setprio 3
	s_mul_i32 s16, s2, 60
	v_and_b32_e32 v72, 31, v0
	v_mad_u32_u24 v76, v18, 15, s16
	v_min_u32_e32 v1, 15, v72
	v_add_u32_e32 v1, v76, v1
	v_min_i32_e32 v2, 0x186a0, v1
	v_ashrrev_i32_e32 v3, 31, v2
	s_waitcnt lgkmcnt(0)
	v_lshl_add_u64 v[2:3], v[2:3], 2, s[14:15]
	global_load_dword v22, v[2:3], off
	v_lshl_or_b32 v1, v18, 5, v72
	v_lshlrev_b32_e32 v1, 2, v1
	global_load_dword v70, v1, s[18:19]
	v_and_b32_e32 v2, 0xc0, v0
	v_mov_b32_e32 v3, 0
	v_lshlrev_b32_e32 v2, 4, v2
	v_lshl_add_u64 v[4:5], s[6:7], 0, v[2:3]
	v_mul_u32_u24_e32 v75, 15, v18
	s_mov_b32 s18, 0
	s_mov_b64 s[2:3], -1
	v_mbcnt_lo_u32_b32 v19, -1, 0
	v_add_u32_e32 v74, v73, v75
	v_lshlrev_b32_e32 v2, 4, v66
	v_lshlrev_b32_e32 v78, 3, v71
	v_lshlrev_b32_e32 v77, 4, v71
	s_waitcnt vmcnt(1)
	v_readlane_b32 s6, v22, 0
	v_readlane_b32 s7, v22, 16
	s_sub_i32 s17, s7, s6
	s_cmpk_lt_i32 s17, 0x181
	s_cbranch_scc1 .LBB3_10
	v_mbcnt_hi_u32_b32 v6, -1, v19
	v_and_b32_e32 v20, 64, v6
	v_or_b32_e32 v21, 1, v20
	s_mov_b32 s7, 0x64646464
	v_mov_b32_e32 v23, 0x4010400
	v_mov_b32_e32 v24, 0x4030402
	s_branch .LBB3_3
